# baseline (speedup 1.0000x reference)
.Lmy_back_4:
	ds_read_b64_tr_b16 v[54:55], v181 offset:49152
	ds_read_b64_tr_b16 v[56:57], v181 offset:49664
	ds_read_b64_tr_b16 v[96:97], v181 offset:53248
	ds_read_b64_tr_b16 v[98:99], v181 offset:53760
	ds_read_b64_tr_b16 v[58:59], v181 offset:50176
	ds_read_b64_tr_b16 v[60:61], v181 offset:50688
	ds_read_b64_tr_b16 v[62:63], v181 offset:54272
	ds_read_b64_tr_b16 v[64:65], v181 offset:54784
	ds_read_b64_tr_b16 v[100:101], v181 offset:51200
	ds_read_b64_tr_b16 v[102:103], v181 offset:51712
	ds_read_b64_tr_b16 v[104:105], v181 offset:55296
	ds_read_b64_tr_b16 v[106:107], v181 offset:55808
	v_add_f32_e32 v49, v80, v81
	v_cvt_pk_f16_f32 v50, v80, v81
	v_cvt_pk_f16_f32 v51, v82, v83
	v_cvt_pk_f16_f32 v52, v84, v85
	v_cvt_pk_f16_f32 v53, v86, v87
	s_nop 1
	s_waitcnt lgkmcnt(10)
	v_mfma_f32_32x32x16_f16 v[16:31], v[50:53], v[54:57], v[16:31]
	ds_read_b64_tr_b16 v[108:109], v181 offset:52224
	ds_read_b64_tr_b16 v[110:111], v181 offset:52736
	ds_read_b64_tr_b16 v[66:67], v181 offset:56320
	ds_read_b64_tr_b16 v[68:69], v181 offset:56832
	v_add_f32_e32 v49, v82, v49
	v_add_f32_e32 v49, v83, v49
	v_add_f32_e32 v49, v84, v49
	v_add_f32_e32 v49, v85, v49
	v_add_f32_e32 v49, v86, v49
	v_add_f32_e32 v49, v87, v49
	s_waitcnt lgkmcnt(12)
	v_mfma_f32_32x32x16_f16 v[32:47], v[50:53], v[96:99], v[32:47]
	v_add_f32_e32 v49, v88, v49
	v_add_f32_e32 v49, v89, v49
	v_add_f32_e32 v49, v90, v49
	v_add_f32_e32 v49, v91, v49
	v_cvt_pk_f16_f32 v50, v88, v89
	v_cvt_pk_f16_f32 v51, v90, v91
	v_cvt_pk_f16_f32 v52, v92, v93
	v_cvt_pk_f16_f32 v53, v94, v95
	v_add_f32_e32 v49, v92, v49
	s_waitcnt lgkmcnt(10)
	v_mfma_f32_32x32x16_f16 v[16:31], v[50:53], v[58:61], v[16:31]
	v_add_f32_e32 v49, v93, v49
	v_add_f32_e32 v49, v94, v49
	v_add_f32_e32 v49, v95, v49
	v_add_f32_e32 v49, v0, v49
	v_add_f32_e32 v49, v1, v49
	v_add_f32_e32 v49, v2, v49
	v_add_f32_e32 v49, v3, v49
	s_waitcnt lgkmcnt(8)
	v_mfma_f32_32x32x16_f16 v[32:47], v[50:53], v[62:65], v[32:47]
	v_cvt_pk_f16_f32 v0, v0, v1
	v_cvt_pk_f16_f32 v1, v2, v3
	v_cvt_pk_f16_f32 v2, v4, v5
	v_cvt_pk_f16_f32 v3, v6, v7
	v_add_f32_e32 v4, v4, v49
	s_nop 0
	s_waitcnt lgkmcnt(6)
	v_mfma_f32_32x32x16_f16 v[16:31], v[0:3], v[100:103], v[16:31]
	v_add_f32_e32 v4, v5, v4
	v_add_f32_e32 v4, v6, v4
	v_cvt_pk_f16_f32 v5, v14, v15
	s_waitcnt lgkmcnt(4)
	v_mfma_f32_32x32x16_f16 v[32:47], v[0:3], v[104:107], v[32:47]
	v_add_f32_e32 v0, v7, v4
	v_add_f32_e32 v0, v8, v0
	v_add_f32_e32 v0, v9, v0
	v_add_f32_e32 v0, v10, v0
	v_cvt_pk_f16_f32 v2, v8, v9
	v_cvt_pk_f16_f32 v3, v10, v11
	v_cvt_pk_f16_f32 v4, v12, v13
	v_add_f32_e32 v0, v11, v0
	s_waitcnt lgkmcnt(2)
	v_mfma_f32_32x32x16_f16 v[16:31], v[2:5], v[108:111], v[16:31]
	v_add_f32_e32 v0, v12, v0
	v_add_f32_e32 v0, v13, v0
	v_add_f32_e32 v0, v14, v0
	v_add_f32_e32 v0, v15, v0
	v_add_f32_e32 v0, v176, v0
	v_mov_b32_e32 v1, v0
	s_nop 1
	v_permlane32_swap_b32_e32 v0, v1
	s_waitcnt lgkmcnt(0)
	v_mfma_f32_32x32x16_f16 v[32:47], v[2:5], v[66:69], v[32:47]
	s_and_saveexec_b64 s[2:3], s[0:1]
	v_add_f32_e32 v0, v0, v1
	ds_write_b32 v186, v0 offset:57472
	s_or_b64 exec, exec, s[2:3]
	s_waitcnt lgkmcnt(0)
	ds_read_b128 v[0:3], v48 offset:57472
	ds_read_b128 v[4:7], v48 offset:57504
	s_mov_b32 s11, 0
	s_lshl_b64 s[0:1], s[10:11], 22
	s_add_u32 s0, s8, s0
	s_waitcnt lgkmcnt(1)
	v_rcp_f32_e32 v8, v0
	v_rcp_f32_e32 v9, v1
	s_addc_u32 s1, s9, s1
	s_lshl_b32 s2, s23, 12
	v_rcp_f32_e32 v10, v2
	v_rcp_f32_e32 v11, v3
	s_waitcnt lgkmcnt(0)
	v_rcp_f32_e32 v12, v4
	ds_read_b128 v[0:3], v48 offset:57536
	v_rcp_f32_e32 v13, v5
	v_rcp_f32_e32 v14, v6
	v_rcp_f32_e32 v15, v7
	ds_read_b128 v[4:7], v48 offset:57568
	s_add_i32 s6, s2, 0
	v_lshlrev_b32_e32 v48, 1, v189
	v_add3_u32 v48, s6, v191, v48
	v_fma_mixlo_f16 v16, v16, v8, 0
	v_fma_mixlo_f16 v8, v32, v8, 0
	ds_write_b16 v48, v8 offset:59456
	v_fma_mixlo_f16 v8, v17, v9, 0
	ds_write_b16 v48, v8 offset:59520
	v_fma_mixlo_f16 v8, v33, v9, 0
	ds_write_b16 v48, v8 offset:59584
	v_fma_mixlo_f16 v8, v18, v10, 0
	ds_write_b16 v48, v8 offset:59648
	v_fma_mixlo_f16 v8, v34, v10, 0
	ds_write_b16 v48, v8 offset:59712
	v_fma_mixlo_f16 v8, v19, v11, 0
	ds_write_b16 v48, v8 offset:59776
	v_fma_mixlo_f16 v8, v35, v11, 0
	ds_write_b16 v48, v8 offset:59840
	v_fma_mixlo_f16 v8, v20, v12, 0
	ds_write_b16 v48, v8 offset:60416
	v_fma_mixlo_f16 v8, v36, v12, 0
	ds_write_b16 v48, v8 offset:60480
	v_fma_mixlo_f16 v8, v21, v13, 0
	ds_write_b16 v48, v8 offset:60544
	v_fma_mixlo_f16 v8, v37, v13, 0
	s_waitcnt lgkmcnt(11)
	v_rcp_f32_e32 v0, v0
	ds_write_b16 v48, v8 offset:60608
	v_fma_mixlo_f16 v8, v22, v14, 0
	v_rcp_f32_e32 v1, v1
	ds_write_b16 v48, v8 offset:60672
	v_fma_mixlo_f16 v8, v38, v14, 0
	ds_write_b16 v48, v8 offset:60736
	v_fma_mixlo_f16 v8, v23, v15, 0
	v_rcp_f32_e32 v2, v2
	ds_write_b16 v48, v8 offset:60800
	v_fma_mixlo_f16 v8, v39, v15, 0
	ds_write_b16 v48, v8 offset:60864
	v_fma_mixlo_f16 v8, v24, v0, 0
	v_fma_mixlo_f16 v0, v40, v0, 0
	v_rcp_f32_e32 v3, v3
	ds_write_b16 v48, v0 offset:61504
	v_fma_mixlo_f16 v0, v25, v1, 0
	ds_write_b16 v48, v0 offset:61568
	v_fma_mixlo_f16 v0, v41, v1, 0
	s_waitcnt lgkmcnt(14)
	v_rcp_f32_e32 v4, v4
	ds_write_b16 v48, v0 offset:61632
	v_fma_mixlo_f16 v0, v26, v2, 0
	ds_write_b16 v48, v0 offset:61696
	v_fma_mixlo_f16 v0, v42, v2, 0
	v_rcp_f32_e32 v5, v5
	ds_write_b16 v48, v0 offset:61760
	v_fma_mixlo_f16 v0, v27, v3, 0
	ds_write_b16 v48, v0 offset:61824
	v_fma_mixlo_f16 v0, v43, v3, 0
	v_rcp_f32_e32 v6, v6
	ds_write_b16 v48, v0 offset:61888
	v_fma_mixlo_f16 v0, v28, v4, 0
	ds_write_b16 v48, v0 offset:62464
	v_fma_mixlo_f16 v0, v44, v4, 0
	v_rcp_f32_e32 v7, v7
	ds_write_b16 v48, v0 offset:62528
	v_fma_mixlo_f16 v0, v29, v5, 0
	ds_write_b16 v48, v0 offset:62592
	v_fma_mixlo_f16 v0, v45, v5, 0
	ds_write_b16 v48, v0 offset:62656
	v_fma_mixlo_f16 v0, v30, v6, 0
	ds_write_b16 v48, v0 offset:62720
	v_fma_mixlo_f16 v0, v46, v6, 0
	ds_write_b16 v48, v0 offset:62784
	v_fma_mixlo_f16 v0, v31, v7, 0
	ds_write_b16 v48, v0 offset:62848
	v_fma_mixlo_f16 v0, v47, v7, 0
	ds_write_b16 v48, v0 offset:62912
	v_lshrrev_b32_e32 v0, 3, v188
	v_and_b32_e32 v4, 56, v190
	s_lshl_b32 s4, s24, 8
	s_lshl_b32 s5, s22, 9
	ds_write_b16 v48, v16 offset:59392
	ds_write_b16 v48, v8 offset:61440
	v_lshlrev_b32_e32 v1, 7, v0
	v_lshlrev_b32_e32 v2, 1, v4
	s_waitcnt lgkmcnt(0)
	v_add3_u32 v8, s6, v1, v2
	s_or_b32 s4, s4, s5
	v_or_b32_e32 v5, s4, v0
	ds_read_b128 v[0:3], v8 offset:59392
	ds_read_b128 v[16:19], v8 offset:60416
	ds_read_b128 v[20:23], v8 offset:61440
	ds_read_b128 v[24:27], v8 offset:62464
	s_lshl_b32 s7, s20, 6
	v_add_lshl_u32 v5, v5, s21, 8
	v_or3_b32 v4, v5, s7, v4
	s_and_b32 s1, s1, 0xffff
	s_mov_b32 s3, 0x20000
	s_mov_b32 s2, 0x400000
	v_lshlrev_b32_e32 v12, 1, v4
	v_add_u32_e32 v13, 0x1000, v12
	v_add_u32_e32 v14, 0x2000, v12
	v_add_u32_e32 v15, 0x3000, v12
	s_waitcnt lgkmcnt(3)
	buffer_store_dwordx4 v[0:3], v12, s[0:3], 0 offen sc1
	s_waitcnt lgkmcnt(2)
	buffer_store_dwordx4 v[16:19], v13, s[0:3], 0 offen sc1
	s_waitcnt lgkmcnt(1)
	buffer_store_dwordx4 v[20:23], v14, s[0:3], 0 offen sc1
	s_waitcnt lgkmcnt(0)
	buffer_store_dwordx4 v[24:27], v15, s[0:3], 0 offen sc1
	s_endpgm
